# grid barrier: waiting workgroups poll the top-level generation word directly instead of their XCD's forwarded copy (one hop less on release)
# speedup vs baseline: 1.0101x; 1.0008x over previous
.LBB0_476:
	global_atomic_add v3, v[168:169], v187, off sc0
	buffer_inv sc1
	v_cvt_f32_u32_e32 v1, v2
	v_sub_u32_e32 v4, 0, v2
	v_rcp_iflag_f32_e32 v1, v1
	s_nop 0
	v_mul_f32_e32 v1, 0x4f7ffffe, v1
	v_cvt_u32_f32_e32 v1, v1
	v_mul_lo_u32 v4, v4, v1
	v_mul_hi_u32 v4, v1, v4
	v_add_u32_e32 v1, v1, v4
	s_waitcnt vmcnt(1)
	v_mul_hi_u32 v1, v3, v1
	v_mul_lo_u32 v4, v1, v2
	v_sub_u32_e32 v4, v3, v4
	v_add_u32_e32 v5, 1, v1
	v_cmp_ge_u32_e32 vcc, v4, v2
	v_add_u32_e32 v3, 1, v3
	s_nop 0
	v_cndmask_b32_e32 v1, v1, v5, vcc
	v_sub_u32_e32 v5, v4, v2
	v_cndmask_b32_e32 v4, v4, v5, vcc
	v_add_u32_e32 v5, 1, v1
	v_cmp_ge_u32_e32 vcc, v4, v2
	s_nop 1
	v_cndmask_b32_e32 v1, v1, v5, vcc
	v_mul_lo_u32 v4, v2, v1
	v_add_u32_e32 v2, v4, v2
	v_cmp_ne_u32_e32 vcc, v3, v2
	s_and_saveexec_b64 s[2:3], vcc
	s_xor_b64 s[2:3], exec, s[2:3]
	s_cbranch_execz .LBB0_490
	s_waitcnt lgkmcnt(0)
	v_readlane_b32 s98, v254, 44
	v_readlane_b32 s99, v254, 45
	s_nop 4
	global_load_dword v0, v173, s[98:99] sc1
	s_waitcnt vmcnt(0)
	v_cmp_eq_u32_e32 vcc, v0, v1
	s_and_saveexec_b64 s[4:5], vcc
	s_cbranch_execz .LBB0_489
	s_mov_b32 s7, 1
	s_mov_b64 s[8:9], 0
	s_branch .LBB0_480

.LBB0_482:
	v_readlane_b32 s98, v254, 44
	v_readlane_b32 s99, v254, 45
	s_nop 4
	global_load_dword v0, v173, s[98:99] sc1
	s_add_i32 s7, s7, 1
	s_mov_b64 s[18:19], -1
	s_waitcnt vmcnt(0)
	v_cmp_ne_u32_e32 vcc, v0, v1
	s_orn2_b64 s[16:17], vcc, exec
	s_branch .LBB0_479

.LBB0_853:
	global_atomic_add v3, v[168:169], v187, off sc0
	buffer_inv sc1
	v_cvt_f32_u32_e32 v1, v2
	v_sub_u32_e32 v4, 0, v2
	v_rcp_iflag_f32_e32 v1, v1
	s_nop 0
	v_mul_f32_e32 v1, 0x4f7ffffe, v1
	v_cvt_u32_f32_e32 v1, v1
	v_mul_lo_u32 v4, v4, v1
	v_mul_hi_u32 v4, v1, v4
	v_add_u32_e32 v1, v1, v4
	s_waitcnt vmcnt(1)
	v_mul_hi_u32 v1, v3, v1
	v_mul_lo_u32 v4, v1, v2
	v_sub_u32_e32 v4, v3, v4
	v_add_u32_e32 v5, 1, v1
	v_cmp_ge_u32_e32 vcc, v4, v2
	v_add_u32_e32 v3, 1, v3
	s_nop 0
	v_cndmask_b32_e32 v1, v1, v5, vcc
	v_sub_u32_e32 v5, v4, v2
	v_cndmask_b32_e32 v4, v4, v5, vcc
	v_add_u32_e32 v5, 1, v1
	v_cmp_ge_u32_e32 vcc, v4, v2
	s_nop 1
	v_cndmask_b32_e32 v1, v1, v5, vcc
	v_mul_lo_u32 v4, v2, v1
	v_add_u32_e32 v2, v4, v2
	v_cmp_ne_u32_e32 vcc, v3, v2
	s_and_saveexec_b64 s[2:3], vcc
	s_xor_b64 s[2:3], exec, s[2:3]
	s_cbranch_execz .LBB0_867
	s_waitcnt lgkmcnt(0)
	v_readlane_b32 s98, v254, 44
	v_readlane_b32 s99, v254, 45
	s_nop 4
	global_load_dword v0, v173, s[98:99] sc1
	s_waitcnt vmcnt(0)
	v_cmp_eq_u32_e32 vcc, v0, v1
	s_and_saveexec_b64 s[8:9], vcc
	s_cbranch_execz .LBB0_866
	s_mov_b32 s12, 1
	s_mov_b64 s[10:11], 0
	s_branch .LBB0_857

.LBB0_859:
	v_readlane_b32 s98, v254, 44
	v_readlane_b32 s99, v254, 45
	s_nop 4
	global_load_dword v0, v173, s[98:99] sc1
	s_add_i32 s12, s12, 1
	s_mov_b64 s[20:21], -1
	s_waitcnt vmcnt(0)
	v_cmp_ne_u32_e32 vcc, v0, v1
	s_orn2_b64 s[18:19], vcc, exec
	s_branch .LBB0_856

.LBB0_1197:
	global_atomic_add v3, v[168:169], v187, off sc0
	buffer_inv sc1
	v_cvt_f32_u32_e32 v1, v2
	v_sub_u32_e32 v4, 0, v2
	v_rcp_iflag_f32_e32 v1, v1
	s_nop 0
	v_mul_f32_e32 v1, 0x4f7ffffe, v1
	v_cvt_u32_f32_e32 v1, v1
	v_mul_lo_u32 v4, v4, v1
	v_mul_hi_u32 v4, v1, v4
	v_add_u32_e32 v1, v1, v4
	s_waitcnt vmcnt(1)
	v_mul_hi_u32 v1, v3, v1
	v_mul_lo_u32 v4, v1, v2
	v_sub_u32_e32 v4, v3, v4
	v_add_u32_e32 v5, 1, v1
	v_cmp_ge_u32_e32 vcc, v4, v2
	v_add_u32_e32 v3, 1, v3
	s_nop 0
	v_cndmask_b32_e32 v1, v1, v5, vcc
	v_sub_u32_e32 v5, v4, v2
	v_cndmask_b32_e32 v4, v4, v5, vcc
	v_add_u32_e32 v5, 1, v1
	v_cmp_ge_u32_e32 vcc, v4, v2
	s_nop 1
	v_cndmask_b32_e32 v1, v1, v5, vcc
	v_mul_lo_u32 v4, v2, v1
	v_add_u32_e32 v2, v4, v2
	v_cmp_ne_u32_e32 vcc, v3, v2
	s_and_saveexec_b64 s[2:3], vcc
	s_xor_b64 s[2:3], exec, s[2:3]
	s_cbranch_execz .LBB0_1211
	s_waitcnt lgkmcnt(0)
	v_readlane_b32 s98, v254, 44
	v_readlane_b32 s99, v254, 45
	s_nop 4
	global_load_dword v0, v173, s[98:99] sc1
	s_waitcnt vmcnt(0)
	v_cmp_eq_u32_e32 vcc, v0, v1
	s_and_saveexec_b64 s[8:9], vcc
	s_cbranch_execz .LBB0_1210
	s_mov_b32 s7, 1
	s_mov_b64 s[10:11], 0
	s_branch .LBB0_1201

.LBB0_1203:
	v_readlane_b32 s98, v254, 44
	v_readlane_b32 s99, v254, 45
	s_nop 4
	global_load_dword v0, v173, s[98:99] sc1
	s_add_i32 s7, s7, 1
	s_mov_b64 s[20:21], -1
	s_waitcnt vmcnt(0)
	v_cmp_ne_u32_e32 vcc, v0, v1
	s_orn2_b64 s[18:19], vcc, exec
	s_branch .LBB0_1200

.LBB0_1393:
	v_readlane_b32 s98, v254, 44
	v_readlane_b32 s99, v254, 45
	s_nop 4
	global_load_dword v0, v173, s[98:99] sc1
	s_add_i32 s7, s7, 1
	s_mov_b64 s[16:17], -1
	s_waitcnt vmcnt(0)
	v_cmp_ne_u32_e32 vcc, v0, v1
	s_orn2_b64 s[14:15], vcc, exec
	s_branch .LBB0_1390

.LBB0_1623:
	v_readlane_b32 s98, v254, 44
	v_readlane_b32 s99, v254, 45
	s_nop 4
	global_load_dword v0, v173, s[98:99] sc1
	s_add_i32 s7, s7, 1
	s_mov_b64 s[26:27], -1
	s_waitcnt vmcnt(0)
	v_cmp_ne_u32_e32 vcc, v0, v1
	s_orn2_b64 s[24:25], vcc, exec
	s_branch .LBB0_1620

.LBB0_1903:
	v_readlane_b32 s98, v254, 44
	v_readlane_b32 s99, v254, 45
	s_nop 4
	global_load_dword v0, v173, s[98:99] sc1
	s_add_i32 s7, s7, 1
	s_mov_b64 s[14:15], -1
	s_waitcnt vmcnt(0)
	v_cmp_ne_u32_e32 vcc, v0, v1
	s_orn2_b64 s[12:13], vcc, exec
	s_branch .LBB0_1900
